# speedup vs baseline: 1.1088x; 1.0057x over previous
.LBB1_17:
	v_lshlrev_b32_e32 v107, 2, v114
	v_add_u32_e32 v107, 0x21000, v107
	global_load_dword v107, v107, s[22:23]
	s_mul_i32 s16, s66, 15
	s_lshl_b32 s14, s67, 3
	s_addk_i32 s16, 0x48
	s_add_i32 s6, s16, s14
	s_lshl_b32 s6, s6, 6
	v_or_b32_e32 v66, s6, v100
	v_mov_b32_e32 v67, 0
	v_lshl_add_u64 v[68:69], v[66:67], 4, s[22:23]
	global_load_dwordx4 v[70:73], v[68:69], off
	s_add_i32 s7, s6, 64
	v_or_b32_e32 v66, s7, v100
	v_lshl_add_u64 v[68:69], v[66:67], 4, s[22:23]
	global_load_dwordx4 v[74:77], v[68:69], off
	s_add_i32 s7, s6, 0x80
	v_or_b32_e32 v66, s7, v100
	v_lshl_add_u64 v[68:69], v[66:67], 4, s[22:23]
	global_load_dwordx4 v[78:81], v[68:69], off
	s_addk_i32 s6, 0xc0
	v_or_b32_e32 v66, s6, v100
	v_lshl_add_u64 v[68:69], v[66:67], 4, s[22:23]
	global_load_dwordx4 v[82:85], v[68:69], off
	s_add_i32 s7, s6, 64
	v_or_b32_e32 v66, s7, v100
	v_lshl_add_u64 v[68:69], v[66:67], 4, s[22:23]
	global_load_dwordx4 v[108:111], v[68:69], off
	s_add_i32 s7, s6, 0x80
	v_or_b32_e32 v66, s7, v100
	v_lshl_add_u64 v[68:69], v[66:67], 4, s[22:23]
	global_load_dwordx4 v[118:121], v[68:69], off
	s_add_i32 s7, s6, 0xc0
	v_or_b32_e32 v66, s7, v100
	v_lshl_add_u64 v[68:69], v[66:67], 4, s[22:23]
	global_load_dwordx4 v[122:125], v[68:69], off
	s_and_b64 s[74:75], vcc, exec
	s_movk_i32 s7, 0x100
	s_cselect_b32 s7, 0xc0, s7
	s_add_i32 s7, s6, s7
	v_or_b32_e32 v66, s7, v100
	v_lshl_add_u64 v[112:113], v[66:67], 4, s[22:23]
	s_mul_i32 s66, s66, 48
	v_mul_u32_u24_e32 v69, 0xd0, v115
	v_mul_u32_u24_e32 v66, 0xd0, v103
	v_mul_u32_u24_e32 v86, 0xd0, v106
	s_movk_i32 s8, 0x9c0
	v_add3_u32 v68, v66, s66, v69
	v_add3_u32 v66, v86, s66, v69
	v_mad_u32_u24 v94, v115, s8, v68
	s_and_b64 s[6:7], vcc, exec
	v_mad_u32_u24 v96, v115, s8, v66
	v_cndmask_b32_e32 v95, v68, v94, vcc
	s_cselect_b32 s6, 0x1b0, 0
	v_cndmask_b32_e32 v97, v66, v96, vcc
	v_add_u32_e32 v86, s6, v95
	v_add_u32_e32 v90, s6, v97
	s_waitcnt lgkmcnt(0)
	s_barrier
	ds_read_b128 v[86:89], v86
	ds_read_b128 v[90:93], v90
	s_movk_i32 s7, 0x1530
	s_cselect_b32 s7, s7, 0xa90
	s_cselect_b32 s9, 32, 0x15f0
	s_movk_i32 s12, 0xab0
	s_cselect_b32 s12, s12, 0x1a0
	s_waitcnt vmcnt(6) lgkmcnt(1)
	v_mfma_f32_32x32x16_f16 v[18:33], v[70:73], v[86:89], v[18:33]
	v_add_u32_e32 v86, s7, v68
	ds_read_b128 v[86:89], v86
	s_waitcnt lgkmcnt(1)
	v_mfma_f32_32x32x16_f16 v[2:17], v[70:73], v[90:93], v[2:17]
	v_add_u32_e32 v90, s7, v66
	ds_read_b128 v[90:93], v90
	s_waitcnt vmcnt(5) lgkmcnt(1)
	v_mfma_f32_32x32x16_f16 v[18:33], v[74:77], v[86:89], v[18:33]
	v_add_u32_e32 v86, s9, v68
	ds_read_b128 v[86:89], v86
	s_waitcnt lgkmcnt(1)
	v_mfma_f32_32x32x16_f16 v[2:17], v[74:77], v[90:93], v[2:17]
	v_add_u32_e32 v90, s9, v66
	ds_read_b128 v[90:93], v90
	s_waitcnt vmcnt(4) lgkmcnt(1)
	v_mfma_f32_32x32x16_f16 v[18:33], v[78:81], v[86:89], v[18:33]
	v_cndmask_b32_e32 v86, v94, v68, vcc
	v_add_u32_e32 v86, s12, v86
	ds_read_b128 v[86:89], v86
	s_waitcnt lgkmcnt(1)
	v_mfma_f32_32x32x16_f16 v[2:17], v[78:81], v[90:93], v[2:17]
	v_cndmask_b32_e32 v90, v96, v66, vcc
	v_add_u32_e32 v90, s12, v90
	ds_read_b128 v[90:93], v90
	s_waitcnt vmcnt(3) lgkmcnt(1)
	v_mfma_f32_32x32x16_f16 v[18:33], v[82:85], v[86:89], v[18:33]
	v_mul_u32_u24_e32 v86, 0xd0, v104
	v_mul_u32_u24_e32 v87, 0xd0, v105
	v_add3_u32 v94, v86, s66, v69
	v_add3_u32 v69, v87, s66, v69
	v_mad_u32_u24 v96, v115, s8, v94
	v_mad_u32_u24 v103, v115, s8, v69
	s_waitcnt lgkmcnt(0)
	v_mfma_f32_32x32x16_f16 v[2:17], v[82:85], v[90:93], v[2:17]
	v_cndmask_b32_e32 v104, v94, v96, vcc
	v_cndmask_b32_e32 v105, v69, v103, vcc
	v_add_u32_e32 v86, s6, v104
	v_add_u32_e32 v90, s6, v105
	ds_read_b128 v[86:89], v86
	ds_read_b128 v[90:93], v90
	s_waitcnt lgkmcnt(1)
	v_mfma_f32_32x32x16_f16 v[50:65], v[70:73], v[86:89], v[50:65]
	v_add_u32_e32 v86, s7, v69
	ds_read_b128 v[86:89], v86
	s_waitcnt lgkmcnt(1)
	v_mfma_f32_32x32x16_f16 v[34:49], v[70:73], v[90:93], v[34:49]
	v_add_u32_e32 v70, s7, v94
	ds_read_b128 v[70:73], v70
	s_waitcnt lgkmcnt(0)
	v_mfma_f32_32x32x16_f16 v[50:65], v[74:77], v[70:73], v[50:65]
	v_add_u32_e32 v70, s9, v94
	ds_read_b128 v[70:73], v70
	v_mfma_f32_32x32x16_f16 v[34:49], v[74:77], v[86:89], v[34:49]
	global_load_dwordx4 v[86:89], v[112:113], off
	v_add_u32_e32 v74, s9, v69
	ds_read_b128 v[74:77], v74
	s_waitcnt lgkmcnt(1)
	v_mfma_f32_32x32x16_f16 v[50:65], v[78:81], v[70:73], v[50:65]
	v_cndmask_b32_e32 v70, v96, v94, vcc
	v_add_u32_e32 v70, s12, v70
	ds_read_b128 v[70:73], v70
	s_waitcnt lgkmcnt(1)
	v_mfma_f32_32x32x16_f16 v[34:49], v[78:81], v[74:77], v[34:49]
	v_cndmask_b32_e32 v74, v103, v69, vcc
	v_add_u32_e32 v74, s12, v74
	ds_read_b128 v[74:77], v74
	s_waitcnt lgkmcnt(1)
	v_mfma_f32_32x32x16_f16 v[50:65], v[82:85], v[70:73], v[50:65]
	s_waitcnt lgkmcnt(0)
	v_mfma_f32_32x32x16_f16 v[34:49], v[82:85], v[74:77], v[34:49]
	s_movk_i32 s24, 0x1610
	s_and_b64 s[16:17], vcc, exec
	s_cselect_b32 s16, s24, 0x1520
	v_add_u32_e32 v78, s16, v68
	ds_read_b128 v[78:81], v78
	v_add_u32_e32 v82, s16, v66
	ds_read_b128 v[82:85], v82
	s_cselect_b32 s6, 0x1c0, 16
	s_movk_i32 s7, 0x1540
	s_cselect_b32 s7, s7, 0xaa0
	s_movk_i32 s8, 0x1600
	s_cselect_b32 s8, 0x1540, s8
	s_waitcnt vmcnt(3) lgkmcnt(1)
	v_mfma_f32_32x32x16_f16 v[18:33], v[108:111], v[78:81], v[18:33]
	v_add_u32_e32 v70, s6, v95
	ds_read_b128 v[70:73], v70
	s_waitcnt lgkmcnt(1)
	v_mfma_f32_32x32x16_f16 v[2:17], v[108:111], v[82:85], v[2:17]
	v_add_u32_e32 v82, s6, v97
	ds_read_b128 v[82:85], v82
	s_waitcnt vmcnt(2) lgkmcnt(1)
	v_mfma_f32_32x32x16_f16 v[18:33], v[118:121], v[70:73], v[18:33]
	v_add_u32_e32 v90, s7, v68
	ds_read_b128 v[90:93], v90
	v_add_u32_e32 v68, s8, v68
	s_waitcnt lgkmcnt(1)
	v_mfma_f32_32x32x16_f16 v[2:17], v[118:121], v[82:85], v[2:17]
	v_add_u32_e32 v82, s7, v66
	ds_read_b128 v[82:85], v82
	v_add_u32_e32 v66, s8, v66
	s_waitcnt vmcnt(0) lgkmcnt(1)
	v_mfma_f32_32x32x16_f16 v[18:33], v[122:125], v[90:93], v[18:33]
	s_cbranch_vccnz .Lmy_p4a_nh1
	ds_read_b128 v[90:93], v68
	s_waitcnt lgkmcnt(1)
	v_mfma_f32_32x32x16_f16 v[2:17], v[122:125], v[82:85], v[2:17]
	ds_read_b128 v[82:85], v66
	s_waitcnt lgkmcnt(1)
	v_mfma_f32_32x32x16_f16 v[18:33], v[86:89], v[90:93], v[18:33]
	s_waitcnt lgkmcnt(0)
	v_mfma_f32_32x32x16_f16 v[2:17], v[86:89], v[82:85], v[2:17]
	s_branch .Lmy_p4a_done
.Lmy_p4a_nh1:
	s_waitcnt lgkmcnt(0)
	v_mfma_f32_32x32x16_f16 v[2:17], v[122:125], v[82:85], v[2:17]
.Lmy_p4a_done:
	v_add_u32_e32 v70, s16, v94
	v_add_u32_e32 v74, s16, v69
	ds_read_b128 v[70:73], v70
	ds_read_b128 v[74:77], v74
	s_waitcnt lgkmcnt(1)
	v_mfma_f32_32x32x16_f16 v[50:65], v[108:111], v[70:73], v[50:65]
	v_add_u32_e32 v70, s6, v104
	ds_read_b128 v[70:73], v70
	s_waitcnt lgkmcnt(1)
	v_mfma_f32_32x32x16_f16 v[34:49], v[108:111], v[74:77], v[34:49]
	v_add_u32_e32 v74, s6, v105
	ds_read_b128 v[74:77], v74
	s_waitcnt lgkmcnt(1)
	v_mfma_f32_32x32x16_f16 v[50:65], v[118:121], v[70:73], v[50:65]
	v_add_u32_e32 v70, s7, v94
	ds_read_b128 v[70:73], v70
	s_waitcnt lgkmcnt(1)
	v_mfma_f32_32x32x16_f16 v[34:49], v[118:121], v[74:77], v[34:49]
	v_add_u32_e32 v74, s7, v69
	ds_read_b128 v[74:77], v74
	s_waitcnt lgkmcnt(1)
	v_mfma_f32_32x32x16_f16 v[50:65], v[122:125], v[70:73], v[50:65]
	s_cbranch_vccnz .Lmy_p4b_nh1
	v_add_u32_e32 v70, s8, v94
	ds_read_b128 v[70:73], v70
	s_waitcnt lgkmcnt(1)
	v_mfma_f32_32x32x16_f16 v[34:49], v[122:125], v[74:77], v[34:49]
	v_add_u32_e32 v74, s8, v69
	ds_read_b128 v[74:77], v74
	s_waitcnt lgkmcnt(1)
	v_mfma_f32_32x32x16_f16 v[50:65], v[86:89], v[70:73], v[50:65]
	s_waitcnt lgkmcnt(0)
	v_mfma_f32_32x32x16_f16 v[34:49], v[86:89], v[74:77], v[34:49]
	s_branch .Lmy_p4b_done
.Lmy_p4b_nh1:
	s_waitcnt lgkmcnt(0)
	v_mfma_f32_32x32x16_f16 v[34:49], v[122:125], v[74:77], v[34:49]
.Lmy_p4b_done:
	s_cmpk_lt_i32 s2, 0x200
	s_movk_i32 s8, 0xd3
	s_cselect_b64 s[6:7], -1, 0
	v_cmp_gt_u32_e32 vcc, s8, v0
	s_and_b64 s[8:9], s[6:7], vcc
	s_barrier
	s_and_saveexec_b64 s[6:7], s[8:9]
	s_cbranch_execz .LBB1_19
	s_add_i32 s8, s2, 0x200
	s_mul_hi_i32 s9, s8, 0x6978
	s_mulk_i32 s8, 0x6978
	s_add_u32 s8, s20, s8
	s_addc_u32 s9, s21, s9
	v_lshlrev_b32_e32 v14, 7, v0
	global_load_dword v67, v14, s[8:9]
.LBB1_19:
	s_or_b64 exec, exec, s[6:7]
	s_mul_i32 s9, s42, 0x79
	v_bfe_u32 v15, v107, 0, 8
	v_add_u32_e32 v15, s9, v15
	v_lshlrev_b32_e32 v14, 3, v115
	v_mul_u32_u24_e32 v15, 48, v15
	v_or_b32_e32 v15, v14, v15
	v_cvt_pk_f16_f32 v17, v20, v21
	v_cvt_pk_f16_f32 v16, v18, v19
	v_cvt_pk_f16_f32 v19, v24, v25
	v_cvt_pk_f16_f32 v18, v22, v23
	ds_write2_b64 v15, v[16:17], v[18:19] offset1:2
	v_cvt_pk_f16_f32 v17, v28, v29
	v_cvt_pk_f16_f32 v16, v26, v27
	ds_write_b64 v15, v[16:17] offset:32
	v_bfe_u32 v15, v107, 8, 8
	v_add_u32_e32 v15, s9, v15
	v_mul_u32_u24_e32 v15, 48, v15
	v_or_b32_e32 v15, v14, v15
	v_cvt_pk_f16_f32 v5, v4, v5
	v_cvt_pk_f16_f32 v4, v2, v3
	v_cvt_pk_f16_f32 v3, v8, v9
	v_cvt_pk_f16_f32 v2, v6, v7
	ds_write2_b64 v15, v[4:5], v[2:3] offset1:2
	v_cvt_pk_f16_f32 v3, v12, v13
	v_cvt_pk_f16_f32 v2, v10, v11
	ds_write_b64 v15, v[2:3] offset:32
	v_bfe_u32 v2, v107, 16, 8
	v_add_u32_e32 v2, s9, v2
	v_mul_u32_u24_e32 v2, 48, v2
	s_movk_i32 s8, 0x79
	v_or_b32_e32 v6, v14, v2
	v_cvt_pk_f16_f32 v3, v52, v53
	v_cvt_pk_f16_f32 v2, v50, v51
	v_cvt_pk_f16_f32 v5, v56, v57
	v_cvt_pk_f16_f32 v4, v54, v55
	ds_write2_b64 v6, v[2:3], v[4:5] offset1:2
	v_cvt_pk_f16_f32 v3, v60, v61
	v_cvt_pk_f16_f32 v2, v58, v59
	v_bfe_u32 v15, v107, 24, 8
	v_cmp_gt_u32_e32 vcc, s8, v15
	ds_write_b64 v6, v[2:3] offset:32
	s_and_saveexec_b64 s[6:7], vcc
	s_cbranch_execz .LBB1_21
	v_add_u32_e32 v2, s9, v15
	v_mul_u32_u24_e32 v2, 48, v2
	v_or_b32_e32 v6, v14, v2
	v_cvt_pk_f16_f32 v3, v36, v37
	v_cvt_pk_f16_f32 v2, v34, v35
	v_cvt_pk_f16_f32 v5, v40, v41
	v_cvt_pk_f16_f32 v4, v38, v39
	ds_write2_b64 v6, v[2:3], v[4:5] offset1:2
	v_cvt_pk_f16_f32 v3, v44, v45
	v_cvt_pk_f16_f32 v2, v42, v43
	ds_write_b64 v6, v[2:3] offset:32

.LBB1_55:
	s_setprio 2
	v_lshrrev_b32_e32 v12, 1, v0
	v_and_b32_e32 v13, 3, v0
	v_and_or_b32 v17, v12, 12, v13
	v_and_b32_e32 v16, 16, v1
	s_lshl_b32 s7, s42, 5
	s_movk_i32 s6, 0x50
	v_or3_b32 v16, v17, v16, s7
	v_mul_u32_u24_e32 v14, s6, v16
	v_add_u32_e32 v16, 0xf550, v14
	v_add_u32_e32 v82, v16, v116
	ds_read_b128 v[38:41], v82
	ds_read_b128 v[110:113], v82 offset:32
	s_movk_i32 s7, 0x500
	s_waitcnt vmcnt(0) lgkmcnt(1)
	v_mfma_f32_32x32x16_f16 v[18:33], v[38:41], v[2:5], 0
	v_mfma_f32_32x32x16_f16 v[2:17], v[38:41], v[6:9], 0
	s_waitcnt lgkmcnt(0)
	v_mfma_f32_32x32x16_f16 v[2:17], v[110:113], v[54:57], v[2:17]
	v_mfma_f32_32x32x16_f16 v[34:49], v[38:41], v[34:37], 0
	v_mfma_f32_32x32x16_f16 v[34:49], v[110:113], v[58:61], v[34:49]
	v_mfma_f32_32x32x16_f16 v[18:33], v[110:113], v[50:53], v[18:33]
	s_nop 5
	v_or_b32_e32 v57, 11, v71
	v_or_b32_e32 v56, 12, v71
	v_or_b32_e32 v55, 13, v71
	v_or_b32_e32 v54, 14, v71
	v_or_b32_e32 v50, 15, v71
	v_add_f32_e32 v34, v83, v34
	v_add_f32_e32 v34, v34, v75
	v_mul_f32_e32 v34, 0xbfb8aa3b, v34
	v_exp_f32_e32 v34, v34
	v_mov_b32_e32 v51, 0xf550
	v_add_f32_e32 v35, v83, v35
	v_lshl_add_u32 v51, v64, 1, v51
	v_mul_u32_u24_e32 v52, s7, v65
	v_add_f32_e32 v35, v35, v76
	v_add_u32_e32 v80, v51, v52
	v_mul_u32_u24_e32 v52, s6, v70
	v_add_f32_e32 v34, 1.0, v34
	v_mul_f32_e32 v35, 0xbfb8aa3b, v35
	v_add_u32_e32 v75, v51, v52
	v_add_u32_e32 v52, 0x1e0, v52
	v_rcp_f32_e32 v34, v34
	v_exp_f32_e32 v76, v35
	v_add_u32_e32 v51, v51, v52
	ds_read_u16 v52, v80
	ds_read_u16 v53, v75
	ds_read_u16 v58, v75 offset:80
	ds_read_u16 v59, v75 offset:160
	ds_read_u16 v60, v75 offset:240
	ds_read_u16 v61, v75 offset:320
	ds_read_u16 v110, v75 offset:400
	ds_read_u16 v111, v51
	s_waitcnt lgkmcnt(7)
	v_cvt_f32_f16_e32 v52, v52
	v_add_f32_e32 v18, v81, v18
	v_add_f32_e32 v36, v83, v36
	v_mul_f32_e32 v35, v72, v34
	v_mul_f32_e32 v18, v18, v34
	v_add_f32_e32 v34, 1.0, v76
	v_add_f32_e32 v36, v36, v105
	v_rcp_f32_e32 v34, v34
	v_mul_f32_e32 v36, 0xbfb8aa3b, v36
	v_mul_f32_e32 v52, v18, v52
	s_waitcnt lgkmcnt(6)
	v_cvt_f32_f16_e32 v18, v53
	v_exp_f32_e32 v36, v36
	v_add_f32_e32 v19, v81, v19
	v_mul_f32_e32 v19, v19, v34
	v_mul_f32_e32 v53, v19, v18
	v_add_f32_e32 v18, 1.0, v36
	v_rcp_f32_e32 v18, v18
	v_add_f32_e32 v36, v83, v37
	s_waitcnt lgkmcnt(5)
	v_cvt_f32_f16_e32 v19, v58
	v_add_f32_e32 v36, v36, v106
	v_mul_f32_e32 v36, 0xbfb8aa3b, v36
	v_exp_f32_e32 v36, v36
	v_add_f32_e32 v20, v81, v20
	v_fmac_f32_e32 v52, 0, v35
	v_mul_f32_e32 v72, v74, v34
	v_mul_f32_e32 v34, v77, v18
	v_mul_f32_e32 v18, v20, v18
	v_fmac_f32_e32 v53, v52, v72
	v_mul_f32_e32 v76, v35, v72
	v_mul_f32_e32 v58, v18, v19
	v_fmac_f32_e32 v58, v53, v34
	v_mul_f32_e32 v37, v76, v34
	v_add_f32_e32 v34, v83, v38
	v_add_f32_e32 v18, 1.0, v36
	v_add_f32_e32 v34, v34, v107
	v_rcp_f32_e32 v18, v18
	v_mul_f32_e32 v34, 0xbfb8aa3b, v34
	s_waitcnt lgkmcnt(4)
	v_cvt_f32_f16_e32 v19, v59
	v_exp_f32_e32 v34, v34
	v_add_f32_e32 v21, v81, v21
	v_mul_f32_e32 v20, v78, v18
	v_mul_f32_e32 v18, v21, v18
	v_add_f32_e32 v21, v83, v39
	v_mul_f32_e32 v59, v18, v19
	v_add_f32_e32 v18, 1.0, v34
	v_add_f32_e32 v21, v21, v108
	v_rcp_f32_e32 v18, v18
	v_mul_f32_e32 v21, 0xbfb8aa3b, v21
	s_waitcnt lgkmcnt(3)
	v_cvt_f32_f16_e32 v19, v60
	v_exp_f32_e32 v21, v21
	v_add_f32_e32 v22, v81, v22
	v_fmac_f32_e32 v59, v58, v20
	v_mul_f32_e32 v77, v37, v20
	v_mul_f32_e32 v20, v79, v18
	v_mul_f32_e32 v18, v22, v18
	v_mul_f32_e32 v60, v18, v19
	v_add_f32_e32 v18, 1.0, v21
	v_add_f32_e32 v21, v83, v40
	v_add_f32_e32 v21, v21, v109
	v_rcp_f32_e32 v18, v18
	v_mul_f32_e32 v21, 0xbfb8aa3b, v21
	s_waitcnt lgkmcnt(2)
	v_cvt_f32_f16_e32 v19, v61
	v_exp_f32_e32 v21, v21
	v_add_f32_e32 v22, v81, v23
	v_fmac_f32_e32 v60, v59, v20
	v_mul_f32_e32 v39, v77, v20
	v_mul_f32_e32 v20, v102, v18
	v_mul_f32_e32 v18, v22, v18
	v_mul_f32_e32 v61, v18, v19
	v_add_f32_e32 v18, 1.0, v21
	v_add_f32_e32 v21, v83, v41
	v_add_f32_e32 v21, v21, v104
	v_rcp_f32_e32 v18, v18
	v_mul_f32_e32 v21, 0xbfb8aa3b, v21
	s_waitcnt lgkmcnt(1)
	v_cvt_f32_f16_e32 v19, v110
	v_exp_f32_e32 v21, v21
	v_add_f32_e32 v22, v81, v24
	v_fmac_f32_e32 v61, v60, v20
	v_mul_f32_e32 v78, v39, v20
	v_mul_f32_e32 v20, v103, v18
	v_mul_f32_e32 v18, v22, v18
	v_mul_f32_e32 v72, v18, v19
	v_add_f32_e32 v18, 1.0, v21
	v_rcp_f32_e32 v18, v18
	v_add_f32_e32 v21, v81, v25
	v_fmac_f32_e32 v72, v61, v20
	v_mul_f32_e32 v79, v78, v20
	v_mul_f32_e32 v20, v101, v18
	v_mul_f32_e32 v18, v21, v18
	v_add_f32_e32 v21, v83, v42
	v_add_f32_e32 v21, v21, v100
	v_mul_f32_e32 v21, 0xbfb8aa3b, v21
	s_waitcnt lgkmcnt(0)
	v_cvt_f32_f16_e32 v19, v111
	v_exp_f32_e32 v21, v21
	v_add_f32_e32 v36, v83, v43
	v_mul_f32_e32 v41, v79, v20
	v_mul_f32_e32 v74, v18, v19
	v_add_f32_e32 v18, 1.0, v21
	v_fmac_f32_e32 v74, v72, v20
	v_rcp_f32_e32 v18, v18
	ds_read_u16 v19, v51 offset:80
	ds_read_u16 v20, v51 offset:160
	ds_read_u16 v21, v51 offset:240
	ds_read_u16 v22, v51 offset:320
	ds_read_u16 v23, v51 offset:400
	ds_read_u16 v24, v51 offset:480
	ds_read_u16 v25, v51 offset:560
	ds_read_u16 v42, v51 offset:640
	v_add_f32_e32 v36, v36, v98
	s_waitcnt lgkmcnt(7)
	v_cvt_f32_f16_e32 v19, v19
	v_mul_f32_e32 v36, 0xbfb8aa3b, v36
	v_exp_f32_e32 v36, v36
	v_add_f32_e32 v26, v81, v26
	v_mul_f32_e32 v34, v84, v18
	v_mul_f32_e32 v18, v26, v18
	v_mul_f32_e32 v26, v18, v19
	v_add_f32_e32 v18, 1.0, v36
	v_fmac_f32_e32 v26, v74, v34
	v_mul_f32_e32 v84, v41, v34
	v_add_f32_e32 v34, v83, v44
	v_rcp_f32_e32 v18, v18
	v_add_f32_e32 v34, v34, v97
	s_waitcnt lgkmcnt(6)
	v_cvt_f32_f16_e32 v19, v20
	v_mul_f32_e32 v34, 0xbfb8aa3b, v34
	v_exp_f32_e32 v36, v34
	v_add_f32_e32 v27, v81, v27
	v_mul_f32_e32 v20, v85, v18
	v_mul_f32_e32 v18, v27, v18
	v_mul_f32_e32 v34, v18, v19
	s_waitcnt lgkmcnt(5)
	v_cvt_f32_f16_e32 v19, v21
	v_add_f32_e32 v21, v83, v45
	v_add_f32_e32 v18, 1.0, v36
	v_add_f32_e32 v21, v21, v96
	v_rcp_f32_e32 v18, v18
	v_mul_f32_e32 v21, 0xbfb8aa3b, v21
	v_exp_f32_e32 v21, v21
	v_add_f32_e32 v27, v81, v28
	v_fmac_f32_e32 v34, v26, v20
	v_mul_f32_e32 v85, v84, v20
	v_mul_f32_e32 v20, v86, v18
	v_mul_f32_e32 v18, v27, v18
	v_mul_f32_e32 v28, v18, v19
	v_add_f32_e32 v18, 1.0, v21
	v_add_f32_e32 v21, v83, v46
	v_add_f32_e32 v21, v21, v95
	v_rcp_f32_e32 v18, v18
	v_mul_f32_e32 v21, 0xbfb8aa3b, v21
	s_waitcnt lgkmcnt(4)
	v_cvt_f32_f16_e32 v19, v22
	v_exp_f32_e32 v21, v21
	v_add_f32_e32 v22, v81, v29
	v_fmac_f32_e32 v28, v34, v20
	v_mul_f32_e32 v86, v85, v20
	v_mul_f32_e32 v20, v87, v18
	v_mul_f32_e32 v18, v22, v18
	v_mul_f32_e32 v36, v18, v19
	v_add_f32_e32 v18, 1.0, v21
	v_add_f32_e32 v21, v83, v47
	v_add_f32_e32 v21, v21, v93
	v_rcp_f32_e32 v18, v18
	v_mul_f32_e32 v21, 0xbfb8aa3b, v21
	s_waitcnt lgkmcnt(3)
	v_cvt_f32_f16_e32 v19, v23
	v_exp_f32_e32 v21, v21
	v_add_f32_e32 v22, v81, v30
	v_fmac_f32_e32 v36, v28, v20
	v_mul_f32_e32 v87, v86, v20
	v_mul_f32_e32 v20, v92, v18
	v_mul_f32_e32 v18, v22, v18
	v_mul_f32_e32 v38, v18, v19
	v_add_f32_e32 v18, 1.0, v21
	v_add_f32_e32 v21, v83, v48
	v_add_f32_e32 v21, v21, v94
	v_rcp_f32_e32 v18, v18
	v_mul_f32_e32 v21, 0xbfb8aa3b, v21
	s_waitcnt lgkmcnt(2)
	v_cvt_f32_f16_e32 v19, v24
	v_exp_f32_e32 v21, v21
	v_add_f32_e32 v22, v81, v31
	v_fmac_f32_e32 v38, v36, v20
	v_mul_f32_e32 v47, v87, v20
	v_mul_f32_e32 v20, v89, v18
	v_mul_f32_e32 v18, v22, v18
	v_mul_f32_e32 v40, v18, v19
	v_add_f32_e32 v18, 1.0, v21
	v_add_f32_e32 v21, v83, v49
	v_add_f32_e32 v21, v21, v91
	v_rcp_f32_e32 v18, v18
	v_mul_f32_e32 v21, 0xbfb8aa3b, v21
	s_waitcnt lgkmcnt(1)
	v_cvt_f32_f16_e32 v19, v25
	v_exp_f32_e32 v21, v21
	v_add_f32_e32 v22, v81, v32
	v_fmac_f32_e32 v40, v38, v20
	v_mul_f32_e32 v31, v47, v20
	v_mul_f32_e32 v20, v90, v18
	v_mul_f32_e32 v18, v22, v18
	v_mul_f32_e32 v32, v18, v19
	v_add_f32_e32 v18, 1.0, v21
	v_rcp_f32_e32 v18, v18
	s_waitcnt lgkmcnt(0)
	v_cvt_f32_f16_e32 v19, v42
	v_add_f32_e32 v21, v81, v33
	v_fmac_f32_e32 v32, v40, v20
	v_mul_f32_e32 v48, v31, v20
	v_mul_f32_e32 v20, v88, v18
	v_mul_f32_e32 v18, v21, v18
	v_mul_f32_e32 v30, v18, v19
	v_fmac_f32_e32 v30, v32, v20
	v_mul_f32_e32 v49, v48, v20
	s_and_saveexec_b64 s[6:7], s[0:1]
	s_cbranch_execz .LBB1_57
	v_add_f32_e32 v2, 0, v2
	v_add_f32_e32 v2, v2, v3
	v_add_f32_e32 v2, v2, v4
	v_add_f32_e32 v2, v2, v5
	v_add_f32_e32 v2, v2, v6
	v_add_f32_e32 v2, v2, v7
	v_add_f32_e32 v2, v2, v8
	v_add_f32_e32 v2, v2, v9
	v_add_f32_e32 v2, v2, v10
	v_add_f32_e32 v2, v2, v11
	v_add_f32_e32 v2, v2, v12
	v_add_f32_e32 v2, v2, v13
	v_add_f32_e32 v2, v2, v14
	v_mul_u32_u24_e32 v3, 21, v65
	v_add_f32_e32 v2, v2, v15
	v_add_lshl_u32 v3, v3, v114, 2
	v_add_f32_e32 v2, v2, v16
	v_add_u32_e32 v4, 0x12450, v3
	v_add_f32_e32 v2, v2, v17
	ds_write_b32 v4, v49
	v_add_u32_e32 v4, 0x126f0, v3
	v_add_u32_e32 v3, 0x12990, v3
	ds_write_b32 v4, v30
	ds_write_b32 v3, v2

.LBB1_66:
	s_or_b64 exec, exec, s[6:7]
	s_waitcnt lgkmcnt(6)
	v_mfma_f32_32x32x16_f16 v[2:17], v[22:25], v[122:125], v[2:17]
	s_and_saveexec_b64 s[6:7], s[0:1]
	s_cbranch_execz .LBB1_68
	s_waitcnt lgkmcnt(5)
	v_add_f32_e32 v18, 0, v29
	s_waitcnt lgkmcnt(4)
	v_add_f32_e32 v18, v18, v33
	s_waitcnt lgkmcnt(3)
	v_add_f32_e32 v18, v18, v42
	v_lshlrev_b32_e32 v67, 2, v114
	s_waitcnt lgkmcnt(2)
	v_add_f32_e32 v18, v18, v43
	v_or_b32_e32 v89, 2, v71
	v_or_b32_e32 v88, 3, v71
	v_or_b32_e32 v83, 4, v71
	v_or_b32_e32 v82, 5, v71
	v_or_b32_e32 v81, 6, v71
	v_or_b32_e32 v73, 7, v71
	v_or_b32_e32 v66, 8, v71
	v_or_b32_e32 v64, 9, v71
	v_add_f32_e32 v71, v62, v2
	v_add_u32_e32 v2, 0x12bdc, v67
	s_waitcnt lgkmcnt(1)
	v_add_f32_e32 v18, v18, v44
	ds_read_b32 v19, v27 offset:504
	ds_read_u16 v22, v80
	ds_read_u16 v23, v75
	ds_read_u16 v24, v75 offset:80
	ds_read_u16 v25, v75 offset:160
	ds_read_u16 v27, v75 offset:240
	ds_read_u16 v29, v75 offset:320
	ds_read_u16 v33, v75 offset:400
	ds_read_b32 v2, v2
	s_waitcnt lgkmcnt(9)
	v_add_f32_e32 v18, v18, v45
	v_or_b32_e32 v20, 0xb600, v67
	s_movk_i32 s0, 0x540
	s_waitcnt lgkmcnt(8)
	v_add_f32_e32 v42, v18, v19
	v_mad_u64_u32 v[18:19], s[0:1], v65, s0, v[20:21]
	s_movk_i32 s0, 0x54
	s_nop 0
	v_mad_u64_u32 v[20:21], s[8:9], v70, s0, v[20:21]
	ds_read_b32 v19, v20 offset:1176
	s_waitcnt lgkmcnt(1)
	v_add_f32_e32 v2, v42, v2
	v_fmamk_f32 v2, v2, 0x3c064b8a, v69
	v_cvt_f32_f16_e32 v69, v22
	v_max_f32_e32 v2, 0, v2
	v_mul_f32_e32 v2, 0xbfb8aa3b, v2
	v_exp_f32_e32 v2, v2
	v_mul_f32_e32 v21, 0xbfb8aa3b, v69
	v_exp_f32_e32 v22, v21
	v_cvt_f32_f16_e32 v75, v23
	v_add_f32_e32 v2, 1.0, v2
	v_rcp_f32_e32 v21, v2
	v_add_f32_e32 v2, 1.0, v22
	v_rcp_f32_e32 v80, v2
	v_mul_f32_e32 v2, 0xbfb8aa3b, v75
	v_exp_f32_e32 v2, v2
	v_cvt_f32_f16_e32 v91, v24
	v_cvt_f32_f16_e32 v94, v25
	v_cvt_f32_f16_e32 v97, v27
	v_add_f32_e32 v2, 1.0, v2
	v_rcp_f32_e32 v92, v2
	v_mul_f32_e32 v2, 0xbfb8aa3b, v91
	v_exp_f32_e32 v2, v2
	v_fmac_f32_e32 v59, v99, v77
	v_cvt_f32_f16_e32 v100, v29
	v_cvt_f32_f16_e32 v103, v33
	v_add_f32_e32 v2, 1.0, v2
	v_rcp_f32_e32 v95, v2
	v_mul_f32_e32 v2, 0xbfb8aa3b, v94
	v_exp_f32_e32 v2, v2
	ds_read2_b32 v[22:23], v20 offset1:21
	v_add_f32_e32 v90, v62, v3
	v_add_f32_e32 v93, v62, v4
	v_add_f32_e32 v2, 1.0, v2
	v_rcp_f32_e32 v77, v2
	v_mul_f32_e32 v2, 0xbfb8aa3b, v97
	v_exp_f32_e32 v2, v2
	ds_read2_b32 v[24:25], v20 offset0:42 offset1:63
	v_add_f32_e32 v96, v62, v5
	v_add_f32_e32 v98, v62, v6
	v_add_f32_e32 v2, 1.0, v2
	v_rcp_f32_e32 v101, v2
	v_mul_f32_e32 v2, 0xbfb8aa3b, v100
	v_exp_f32_e32 v2, v2
	ds_read2_b32 v[42:43], v20 offset0:84 offset1:105
	v_add_f32_e32 v102, v62, v7
	v_fmac_f32_e32 v72, v99, v79
	v_add_f32_e32 v2, 1.0, v2
	v_rcp_f32_e32 v104, v2
	v_mul_f32_e32 v2, 0xbfb8aa3b, v103
	v_exp_f32_e32 v2, v2
	ds_read_u16 v3, v51
	ds_read_u16 v4, v51 offset:80
	ds_read_u16 v5, v51 offset:160
	ds_read_u16 v6, v51 offset:240
	ds_read_u16 v7, v51 offset:320
	ds_read_u16 v33, v51 offset:400
	ds_read_u16 v79, v51 offset:480
	ds_read_u16 v106, v51 offset:560
	s_waitcnt lgkmcnt(7)
	v_cvt_f32_f16_e32 v107, v3
	s_waitcnt lgkmcnt(6)
	v_cvt_f32_f16_e32 v27, v4
	v_add_f32_e32 v2, 1.0, v2
	v_rcp_f32_e32 v108, v2
	v_mul_f32_e32 v2, 0xbfb8aa3b, v107
	v_exp_f32_e32 v2, v2
	v_fmac_f32_e32 v52, v99, v35
	s_waitcnt lgkmcnt(5)
	v_cvt_f32_f16_e32 v35, v5
	v_fmac_f32_e32 v26, v99, v84
	v_add_f32_e32 v2, 1.0, v2
	v_rcp_f32_e32 v110, v2
	v_mul_f32_e32 v2, 0xbfb8aa3b, v27
	v_exp_f32_e32 v2, v2
	s_waitcnt lgkmcnt(4)
	v_cvt_f32_f16_e32 v29, v6
	v_fmac_f32_e32 v53, v99, v76
	v_add_f32_e32 v76, v62, v11
	v_add_f32_e32 v2, 1.0, v2
	v_rcp_f32_e32 v84, v2
	v_mul_f32_e32 v2, 0xbfb8aa3b, v35
	v_exp_f32_e32 v2, v2
	v_fmac_f32_e32 v58, v99, v37
	s_waitcnt lgkmcnt(3)
	v_cvt_f32_f16_e32 v37, v7
	v_fmac_f32_e32 v60, v99, v39
	v_add_f32_e32 v2, 1.0, v2
	v_rcp_f32_e32 v11, v2
	v_mul_f32_e32 v2, 0xbfb8aa3b, v29
	v_exp_f32_e32 v2, v2
	v_fmac_f32_e32 v74, v99, v41
	s_waitcnt lgkmcnt(2)
	v_cvt_f32_f16_e32 v39, v33
	s_waitcnt lgkmcnt(1)
	v_cvt_f32_f16_e32 v41, v79
	v_add_f32_e32 v2, 1.0, v2
	v_fmac_f32_e32 v34, v99, v85
	v_rcp_f32_e32 v85, v2
	v_mul_f32_e32 v2, 0xbfb8aa3b, v37
	v_exp_f32_e32 v2, v2
	v_mul_f32_e32 v3, 0xbfb8aa3b, v39
	v_mul_f32_e32 v6, 0xbfb8aa3b, v41
	v_exp_f32_e32 v3, v3
	v_exp_f32_e32 v6, v6
	s_waitcnt lgkmcnt(0)
	v_cvt_f32_f16_e32 v33, v106
	v_add_f32_e32 v2, 1.0, v2
	v_add_f32_e32 v46, v62, v13
	v_rcp_f32_e32 v13, v2
	v_add_f32_e32 v2, 1.0, v3
	v_add_f32_e32 v6, 1.0, v6
	v_fmac_f32_e32 v28, v99, v86
	v_fmac_f32_e32 v36, v99, v87
	v_rcp_f32_e32 v86, v2
	v_add_u32_e32 v2, 0x200, v20
	v_rcp_f32_e32 v87, v6
	v_mul_f32_e32 v6, 0xbfb8aa3b, v33
	v_add_f32_e32 v105, v62, v8
	ds_read2_b32 v[44:45], v20 offset0:126 offset1:147
	v_add_f32_e32 v109, v62, v9
	v_add_f32_e32 v70, v62, v10
	ds_read2_b32 v[8:9], v20 offset0:168 offset1:189
	ds_read2_b32 v[4:5], v20 offset0:210 offset1:231
	ds_read2_b32 v[2:3], v2 offset0:124 offset1:145
	v_add_f32_e32 v10, v62, v15
	v_exp_f32_e32 v6, v6
	ds_read_b32 v15, v18
	ds_read_u16 v7, v51 offset:640
	v_mov_b32_e32 v20, v17
	v_fmac_f32_e32 v40, v99, v31
	v_add_f32_e32 v6, 1.0, v6
	v_rcp_f32_e32 v18, v6
	s_waitcnt lgkmcnt(0)
	v_cvt_f32_f16_e32 v31, v7
	v_pk_add_f32 v[6:7], v[62:63], v[20:21]
	v_fmac_f32_e32 v61, v99, v78
	v_add_f32_e32 v78, v62, v12
	v_add_f32_e32 v12, v62, v16
	v_mul_f32_e32 v16, v7, v69
	v_fmac_f32_e32 v16, v71, v52
	v_fmac_f32_e32 v15, v16, v80
	v_mul_f32_e32 v16, v7, v75
	v_fmac_f32_e32 v16, v90, v53
	v_add_f32_e32 v15, 0, v15
	v_fma_f32 v16, v16, v92, v22
	v_add_f32_e32 v15, v15, v16
	v_mul_f32_e32 v16, v7, v91
	s_movk_i32 s1, 0x7a
	v_fmac_f32_e32 v16, v93, v58
	v_fmac_f32_e32 v23, v16, v95
	v_cmp_gt_u32_e32 vcc, s1, v89
	v_mov_b32_e32 v71, v7
	v_mov_b32_e32 v79, v7
	v_cndmask_b32_e32 v16, 0, v23, vcc
	v_add_f32_e32 v15, v15, v16
	v_mul_f32_e32 v16, v7, v94
	v_fmac_f32_e32 v16, v96, v59
	v_fma_f32 v16, v16, v77, v24
	v_cmp_gt_u32_e32 vcc, s1, v88
	v_mov_b32_e32 v77, v7
	v_fmac_f32_e32 v38, v99, v47
	v_cndmask_b32_e32 v16, 0, v16, vcc
	v_add_f32_e32 v15, v15, v16
	v_mul_f32_e32 v16, v7, v97
	v_fmac_f32_e32 v16, v98, v60
	v_fmac_f32_e32 v25, v16, v101
	v_cmp_gt_u32_e32 vcc, s1, v83
	v_mov_b32_e32 v47, v7
	v_add_f32_e32 v14, v62, v14
	v_cndmask_b32_e32 v16, 0, v25, vcc
	v_add_f32_e32 v15, v15, v16
	v_mul_f32_e32 v16, v7, v100
	v_fmac_f32_e32 v16, v102, v61
	v_fma_f32 v16, v16, v104, v42
	v_cmp_gt_u32_e32 vcc, s1, v82
	v_fmac_f32_e32 v32, v99, v48
	v_fmac_f32_e32 v30, v99, v49
	v_cndmask_b32_e32 v16, 0, v16, vcc
	v_add_f32_e32 v15, v15, v16
	v_mul_f32_e32 v16, v7, v103
	v_fmac_f32_e32 v16, v105, v72
	v_fmac_f32_e32 v43, v16, v108
	v_cmp_gt_u32_e32 vcc, s1, v81
	s_nop 1
	v_cndmask_b32_e32 v16, 0, v43, vcc
	v_add_f32_e32 v15, v15, v16
	v_mul_f32_e32 v16, v7, v107
	v_fmac_f32_e32 v16, v109, v74
	v_fma_f32 v16, v16, v110, v44
	v_cmp_gt_u32_e32 vcc, s1, v73
	s_nop 1
	v_cndmask_b32_e32 v16, 0, v16, vcc
	v_add_f32_e32 v15, v15, v16
	v_pk_mul_f32 v[16:17], v[70:71], v[26:27]
	v_cmp_gt_u32_e32 vcc, s1, v66
	v_add_f32_e32 v16, v16, v17
	v_fmac_f32_e32 v45, v16, v84
	v_cndmask_b32_e32 v16, 0, v45, vcc
	v_add_f32_e32 v15, v15, v16
	v_pk_mul_f32 v[16:17], v[76:77], v[34:35]
	v_cmp_gt_u32_e32 vcc, s1, v64
	v_add_f32_e32 v16, v16, v17
	v_fma_f32 v8, v16, v11, v8
	v_pk_mul_f32 v[16:17], v[78:79], v[28:29]
	v_cndmask_b32_e32 v8, 0, v8, vcc
	v_add_f32_e32 v11, v16, v17
	v_fmac_f32_e32 v9, v11, v85
	v_cmp_gt_u32_e32 vcc, s1, v68
	v_add_f32_e32 v8, v15, v8
	v_mov_b32_e32 v15, v7
	v_cndmask_b32_e32 v9, 0, v9, vcc
	v_add_f32_e32 v11, v8, v9
	v_pk_mul_f32 v[8:9], v[46:47], v[36:37]
	v_cmp_gt_u32_e32 vcc, s1, v57
	v_add_f32_e32 v8, v8, v9
	v_fma_f32 v4, v8, v13, v4
	v_pk_mul_f32 v[8:9], v[14:15], v[38:39]
	v_cndmask_b32_e32 v4, 0, v4, vcc
	v_add_f32_e32 v8, v8, v9
	v_fmac_f32_e32 v5, v8, v86
	v_cmp_gt_u32_e32 vcc, s1, v56
	v_add_f32_e32 v4, v11, v4
	v_mov_b32_e32 v11, v7
	v_cndmask_b32_e32 v5, 0, v5, vcc
	v_add_f32_e32 v8, v4, v5
	v_pk_mul_f32 v[4:5], v[10:11], v[40:41]
	v_mov_b32_e32 v13, v7
	v_add_f32_e32 v4, v4, v5
	v_fma_f32 v2, v4, v87, v2
	v_pk_mul_f32 v[4:5], v[12:13], v[32:33]
	v_cmp_gt_u32_e32 vcc, s1, v55
	v_add_f32_e32 v4, v4, v5
	v_mul_f32_e32 v5, 0xbfb8aa3b, v31
	v_exp_f32_e32 v5, v5
	v_fmac_f32_e32 v3, v4, v18
	v_cndmask_b32_e32 v2, 0, v2, vcc
	v_cmp_gt_u32_e32 vcc, s1, v54
	v_add_f32_e32 v4, 1.0, v5
	v_rcp_f32_e32 v4, v4
	v_add_f32_e32 v2, v8, v2
	v_cndmask_b32_e32 v3, 0, v3, vcc
	v_add_f32_e32 v5, v2, v3
	v_pk_mul_f32 v[2:3], v[6:7], v[30:31]
	v_cmp_gt_u32_e32 vcc, s1, v50
	v_add_f32_e32 v2, v2, v3
	v_fmac_f32_e32 v19, v2, v4
	v_cndmask_b32_e32 v2, 0, v19, vcc
	v_mul_u32_u24_e32 v3, s0, v65
	s_mov_b32 s0, 0x12c30
	v_add_f32_e32 v2, v5, v2
	v_add3_u32 v3, v3, v67, s0
	ds_write_b32 v3, v2
